# conversion split: only 1024 MoE-weight items in the P1 tail (their traffic was slowing the last in-proj round), P2 background takes the other 1024
# speedup vs baseline: 1.0121x; 1.0121x over previous
; #define LAS __attribute__((address_space(3)))
; __device__ __forceinline__ void cvt_fill_g(const Frame& F) { LAS float* gl = (LAS float*)(F.lds + BG_G_OFF); for (int i = F.tid; i < DM; i += NTHREADS) gl[i] = F.g_moe[i] * WSCALE; __syncthreads(); }
;     __device__ __forceinline__ void init(const Frame& F_, int first_item, int n_items) { init(F_, first_item, n_items, F_.vcu, F_.G); }
; __global__ void __launch_bounds__(NTHREADS, 2) mk_fwd(Args args) {
;     ...
;         if (F.G == 256 && blockIdx.x >= 208) {
;             cvt_fill_g(F);
;             Bg bg; bg.init(F, CVT_ITEMS - CVT_P9_ITEMS - CVT_P4_ITEMS - CVT_P1_ITEMS, CVT_P1_ITEMS, (int)blockIdx.x - 208, 48); bg.drain();
.LBB0_281:
	global_load_dword v6, v[2:3], off
	v_add_u32_e32 v5, 0x200, v5
	v_cmp_lt_u32_e32 vcc, s3, v5
	v_lshl_add_u64 v[2:3], v[2:3], 0, s[4:5]
	s_or_b64 s[0:1], vcc, s[0:1]
	s_waitcnt vmcnt(0)
	v_mul_f32_e32 v6, 0x42800000, v6
	ds_write_b32 v4, v6
	v_add_u32_e32 v4, 0x800, v4
	s_andn2_b64 exec, exec, s[0:1]
	s_cbranch_execnz .LBB0_281
	s_or_b64 exec, exec, s[0:1]
	v_readlane_b32 s1, v254, 8
	s_lshl_b32 s0, s2, 2
	s_lshr_b32 s1, s1, 7
	s_add_i32 s3, s0, s1
	s_addk_i32 s3, 0xfcc0
	s_cmpk_gt_i32 s3, 0x3ff
	s_cselect_b64 s[0:1], -1, 0
	s_mov_b32 s34, 0
	s_and_b64 vcc, exec, s[0:1]
	s_waitcnt lgkmcnt(0)
	s_barrier
	s_cbranch_vccnz .LBB0_284
	s_sub_i32 s4, 0x4bf, s3
	s_mul_hi_i32 s4, s4, 0x2aaaaaab
	s_lshr_b32 s5, s4, 31
	s_ashr_i32 s4, s4, 5
	s_add_i32 s4, s4, s5
	s_lshl_b32 s34, s4, 1

; #define LAS __attribute__((address_space(3)))
; __device__ __forceinline__ void cvt_fill_g(const Frame& F) { LAS float* gl = (LAS float*)(F.lds + BG_G_OFF); for (int i = F.tid; i < DM; i += NTHREADS) gl[i] = F.g_moe[i] * WSCALE; __syncthreads(); }
;     __device__ __forceinline__ void init(const Frame& F_, int first_item, int n_items) { init(F_, first_item, n_items, F_.vcu, F_.G); }
; __global__ void __launch_bounds__(NTHREADS, 2) mk_fwd(Args args) {
;     ...
;         cvt_fill_g(F);
;         Bg bg; bg.init(F, CVT_P0_ITEMS, CVT_ITEMS - CVT_P0_ITEMS - (F.G == 256 ? CVT_P9_ITEMS + CVT_P4_ITEMS + CVT_P1_ITEMS : 0));
.LBB0_367:
	global_load_dword v5, v[2:3], off
	v_add_u32_e32 v4, 0x200, v4
	v_cmp_lt_u32_e32 vcc, s3, v4
	v_lshl_add_u64 v[2:3], v[2:3], 0, s[4:5]
	s_or_b64 s[0:1], vcc, s[0:1]
	s_waitcnt vmcnt(0)
	v_mul_f32_e32 v5, 0x42800000, v5
	ds_write_b32 v1, v5
	v_add_u32_e32 v1, 0x800, v1
	s_andn2_b64 exec, exec, s[0:1]
	s_cbranch_execnz .LBB0_367
	s_or_b64 exec, exec, s[0:1]
	s_cmpk_eq_i32 s33, 0x100
	s_movk_i32 s0, 0x4800
	v_readlane_b32 s1, v254, 8
	s_cselect_b32 s0, s0, 0x6000
	s_lshl_b32 s3, s52, 2
	s_lshr_b32 s1, s1, 7
	s_add_i32 s3, s3, s1
	s_addk_i32 s3, 0x400
	s_lshl_b32 s55, s33, 2
	s_cmp_ge_i32 s3, s0
	s_mov_b32 s54, 0
	s_waitcnt lgkmcnt(0)
	s_barrier
	s_cbranch_scc1 .LBB0_370
	s_abs_i32 s1, s55
	v_cvt_f32_u32_e32 v1, s1
	s_add_i32 s0, s55, s0
	s_not_b32 s4, s3
	s_add_i32 s4, s4, s0
	v_rcp_iflag_f32_e32 v1, v1
	s_sub_i32 s0, 0, s1
	s_xor_b32 s5, s4, s55
	s_abs_i32 s4, s4
	v_mul_f32_e32 v1, 0x4f7ffffe, v1
	v_cvt_u32_f32_e32 v1, v1
	s_ashr_i32 s5, s5, 31
	v_readfirstlane_b32 s6, v1
	s_mul_i32 s0, s0, s6
	s_mul_hi_u32 s0, s6, s0
	s_add_i32 s6, s6, s0
	s_mul_hi_u32 s0, s4, s6
	s_mul_i32 s6, s0, s1
	s_sub_i32 s4, s4, s6
	s_add_i32 s7, s0, 1
	s_sub_i32 s6, s4, s1
	s_cmp_ge_u32 s4, s1
	s_cselect_b32 s0, s7, s0
	s_cselect_b32 s4, s6, s4
	s_add_i32 s6, s0, 1
	s_cmp_ge_u32 s4, s1
	s_cselect_b32 s0, s6, s0
	s_xor_b32 s0, s0, s5
	s_sub_i32 s0, s0, s5
	s_lshl_b32 s54, s0, 1
